# speedup vs baseline: 1.0051x; 1.0051x over previous
_Z12front_kernel9FrontArgs8PrepArgs8FragArgs:
	s_load_dwordx16 s[4:19], s[0:1], 0x10
	s_cmpk_gt_i32 s2, 0xff
	s_mov_b64 s[20:21], -1
	s_cbranch_scc0 .LBB1_117
	s_load_dword s3, s[0:1], 0x164
	s_add_u32 s34, s0, 0x60
	s_addc_u32 s35, s1, 0
	s_add_i32 s30, s2, 0xffffff00
	s_waitcnt lgkmcnt(0)
	s_add_i32 s20, s3, 0x1ff
	s_ashr_i32 s21, s20, 31
	s_lshr_b32 s21, s21, 23
	s_add_i32 s20, s20, s21
	s_ashr_i32 s22, s20, 9
	s_cmp_ge_i32 s30, s22
	s_mov_b64 s[20:21], -1
	s_cbranch_scc0 .LBB1_103
	s_load_dword s31, s[0:1], 0x2f4
	s_add_u32 s24, s0, 0x1b0
	s_addc_u32 s25, s1, 0
	s_sub_i32 s33, s30, s22
	s_waitcnt lgkmcnt(0)
	s_add_i32 s20, s31, 7
	s_ashr_i32 s21, s20, 31
	s_lshr_b32 s21, s21, 29
	s_add_i32 s20, s20, s21
	s_ashr_i32 s26, s20, 3
	s_cmp_ge_i32 s33, s26
	s_mov_b64 s[20:21], -1
	s_cbranch_scc0 .LBB1_89
	s_cmp_lg_u32 s33, s26
	s_cbranch_scc0 .LBB1_61
	s_not_b32 s26, s26
	s_add_i32 s38, s33, s26
	s_cmpk_lt_u32 s38, 0x100
	s_cselect_b64 s[28:29], -1, 0
	s_cmpk_gt_u32 s38, 0xff
	s_load_dwordx4 s[20:23], s[0:1], 0x50
	s_cselect_b64 s[26:27], -1, 0
	s_and_b64 s[36:37], s[28:29], exec
	s_cselect_b32 s5, s5, s7
	s_cselect_b32 s4, s4, s6
	s_bfe_u32 s36, s38, 0x20006
	s_lshl_b32 s6, s38, 5
	v_lshrrev_b32_e32 v4, 5, v0
	s_and_b32 s37, s6, 0x7e0
	v_and_b32_e32 v5, 31, v0
	s_mul_i32 s6, s36, 0x180
	v_lshrrev_b32_e32 v4, 5, v0
	v_and_b32_e32 v5, 31, v0
	v_add_u32_e32 v6, s6, v4
	v_lshlrev_b32_e32 v6, 11, v6
	v_add3_u32 v6, v6, s37, v5
	v_lshlrev_b32_e32 v6, 2, v6
	v_mul_u32_u24_e32 v7, 33, v4
	v_add_lshl_u32 v7, v7, v5, 2
	s_mov_b64 s[38:39], s[4:5]
	s_and_b64 s[4:5], s[28:29], exec
	s_cselect_b32 s7, s9, s13
	s_cselect_b32 s6, s8, s12
	s_cselect_b32 s5, s11, s15
	s_cselect_b32 s4, s10, s14
	v_and_b32_e32 v3, 63, v0
	v_mul_u32_u24_e32 v2, 24, v3
	v_lshrrev_b32_e32 v1, 6, v0
	global_load_dwordx4 v[56:59], v2, s[6:7]
	global_load_dwordx2 v[60:61], v2, s[6:7] offset:16
	global_load_dwordx4 v[62:65], v2, s[4:5]
	global_load_dwordx2 v[66:67], v2, s[4:5] offset:16
	global_load_dword v8, v6, s[38:39] nt
	s_add_u32 s38, s38, 0x20000
	s_addc_u32 s39, s39, 0
	global_load_dword v9, v6, s[38:39] nt
	s_add_u32 s38, s38, 0x20000
	s_addc_u32 s39, s39, 0
	global_load_dword v10, v6, s[38:39] nt
	s_add_u32 s38, s38, 0x20000
	s_addc_u32 s39, s39, 0
	global_load_dword v11, v6, s[38:39] nt
	s_add_u32 s38, s38, 0x20000
	s_addc_u32 s39, s39, 0
	global_load_dword v12, v6, s[38:39] nt
	s_add_u32 s38, s38, 0x20000
	s_addc_u32 s39, s39, 0
	global_load_dword v13, v6, s[38:39] nt
	s_add_u32 s38, s38, 0x20000
	s_addc_u32 s39, s39, 0
	global_load_dword v14, v6, s[38:39] nt
	s_add_u32 s38, s38, 0x20000
	s_addc_u32 s39, s39, 0
	global_load_dword v15, v6, s[38:39] nt
	s_add_u32 s38, s38, 0x20000
	s_addc_u32 s39, s39, 0
	global_load_dword v16, v6, s[38:39] nt
	s_add_u32 s38, s38, 0x20000
	s_addc_u32 s39, s39, 0
	global_load_dword v17, v6, s[38:39] nt
	s_add_u32 s38, s38, 0x20000
	s_addc_u32 s39, s39, 0
	global_load_dword v18, v6, s[38:39] nt
	s_add_u32 s38, s38, 0x20000
	s_addc_u32 s39, s39, 0
	global_load_dword v19, v6, s[38:39] nt
	s_add_u32 s38, s38, 0x20000
	s_addc_u32 s39, s39, 0
	global_load_dword v20, v6, s[38:39] nt
	s_add_u32 s38, s38, 0x20000
	s_addc_u32 s39, s39, 0
	global_load_dword v21, v6, s[38:39] nt
	s_add_u32 s38, s38, 0x20000
	s_addc_u32 s39, s39, 0
	global_load_dword v22, v6, s[38:39] nt
	s_add_u32 s38, s38, 0x20000
	s_addc_u32 s39, s39, 0
	global_load_dword v23, v6, s[38:39] nt
	s_add_u32 s38, s38, 0x20000
	s_addc_u32 s39, s39, 0
	global_load_dword v24, v6, s[38:39] nt
	s_add_u32 s38, s38, 0x20000
	s_addc_u32 s39, s39, 0
	global_load_dword v25, v6, s[38:39] nt
	s_add_u32 s38, s38, 0x20000
	s_addc_u32 s39, s39, 0
	global_load_dword v26, v6, s[38:39] nt
	s_add_u32 s38, s38, 0x20000
	s_addc_u32 s39, s39, 0
	global_load_dword v27, v6, s[38:39] nt
	s_add_u32 s38, s38, 0x20000
	s_addc_u32 s39, s39, 0
	global_load_dword v28, v6, s[38:39] nt
	s_add_u32 s38, s38, 0x20000
	s_addc_u32 s39, s39, 0
	global_load_dword v29, v6, s[38:39] nt
	s_add_u32 s38, s38, 0x20000
	s_addc_u32 s39, s39, 0
	global_load_dword v30, v6, s[38:39] nt
	s_add_u32 s38, s38, 0x20000
	s_addc_u32 s39, s39, 0
	global_load_dword v31, v6, s[38:39] nt
	s_waitcnt vmcnt(23)
	ds_write_b32 v7, v8
	s_waitcnt vmcnt(22)
	ds_write_b32 v7, v9 offset:2112
	s_waitcnt vmcnt(21)
	ds_write_b32 v7, v10 offset:4224
	s_waitcnt vmcnt(20)
	ds_write_b32 v7, v11 offset:6336
	s_waitcnt vmcnt(19)
	ds_write_b32 v7, v12 offset:8448
	s_waitcnt vmcnt(18)
	ds_write_b32 v7, v13 offset:10560
	s_waitcnt vmcnt(17)
	ds_write_b32 v7, v14 offset:12672
	s_waitcnt vmcnt(16)
	ds_write_b32 v7, v15 offset:14784
	s_waitcnt vmcnt(15)
	ds_write_b32 v7, v16 offset:16896
	s_waitcnt vmcnt(14)
	ds_write_b32 v7, v17 offset:19008
	s_waitcnt vmcnt(13)
	ds_write_b32 v7, v18 offset:21120
	s_waitcnt vmcnt(12)
	ds_write_b32 v7, v19 offset:23232
	s_waitcnt vmcnt(11)
	ds_write_b32 v7, v20 offset:25344
	s_waitcnt vmcnt(10)
	ds_write_b32 v7, v21 offset:27456
	s_waitcnt vmcnt(9)
	ds_write_b32 v7, v22 offset:29568
	s_waitcnt vmcnt(8)
	ds_write_b32 v7, v23 offset:31680
	s_waitcnt vmcnt(7)
	ds_write_b32 v7, v24 offset:33792
	s_waitcnt vmcnt(6)
	ds_write_b32 v7, v25 offset:35904
	s_waitcnt vmcnt(5)
	ds_write_b32 v7, v26 offset:38016
	s_waitcnt vmcnt(4)
	ds_write_b32 v7, v27 offset:40128
	s_waitcnt vmcnt(3)
	ds_write_b32 v7, v28 offset:42240
	s_waitcnt vmcnt(2)
	ds_write_b32 v7, v29 offset:44352
	s_waitcnt vmcnt(1)
	ds_write_b32 v7, v30 offset:46464
	s_waitcnt vmcnt(0)
	ds_write_b32 v7, v31 offset:48576
	s_waitcnt lgkmcnt(0)
	s_barrier
	v_mul_u32_u24_e32 v68, 0x318, v3
	v_lshl_add_u32 v68, v1, 4, v68
	ds_read_b32 v8, v68
	ds_read_b32 v9, v68 offset:132
	ds_read_b32 v10, v68 offset:264
	ds_read_b32 v11, v68 offset:396
	ds_read_b32 v12, v68 offset:528
	ds_read_b32 v13, v68 offset:660
	ds_read_b32 v16, v68 offset:4
	ds_read_b32 v17, v68 offset:136
	ds_read_b32 v18, v68 offset:268
	ds_read_b32 v19, v68 offset:400
	ds_read_b32 v20, v68 offset:532
	ds_read_b32 v21, v68 offset:664
	ds_read_b32 v24, v68 offset:8
	ds_read_b32 v25, v68 offset:140
	ds_read_b32 v26, v68 offset:272
	ds_read_b32 v27, v68 offset:404
	ds_read_b32 v28, v68 offset:536
	ds_read_b32 v29, v68 offset:668
	ds_read_b32 v32, v68 offset:12
	ds_read_b32 v33, v68 offset:144
	ds_read_b32 v34, v68 offset:276
	ds_read_b32 v35, v68 offset:408
	ds_read_b32 v36, v68 offset:540
	ds_read_b32 v37, v68 offset:672
	s_lshl_b32 s40, s36, 11
	s_or_b32 s40, s40, s37
	v_lshl_add_u32 v69, v1, 2, s40
	v_mul_u32_u24_e32 v70, 12, v3
	v_mov_b32_e32 v71, 0x300
	v_mad_u32_u24 v70, v69, v71, v70
	v_mov_b32_e32 v71, 0x600
	v_mad_u32_u24 v71, v69, v71, v2
	v_add_u32_e32 v72, 0xc00, v71
	s_and_b64 s[40:41], s[28:29], exec
	s_cselect_b32 s42, s18, s20
	s_cselect_b32 s43, s19, s21
	s_waitcnt lgkmcnt(0)
	s_cbranch_scc0 .Lln_nox0
	global_store_dwordx4 v71, v[8:11], s[22:23]
	global_store_dwordx2 v71, v[12:13], s[22:23] offset:16
	global_store_dwordx4 v71, v[16:19], s[22:23] offset:1536
	global_store_dwordx2 v71, v[20:21], s[22:23] offset:1552
	global_store_dwordx4 v72, v[24:27], s[22:23]
	global_store_dwordx2 v72, v[28:29], s[22:23] offset:16
	global_store_dwordx4 v72, v[32:35], s[22:23] offset:1536
	global_store_dwordx2 v72, v[36:37], s[22:23] offset:1552
.Lln_nox0:
	v_add_f32_e32 v73, v8, v9
	v_add_f32_e32 v74, v16, v17
	v_add_f32_e32 v75, v24, v25
	v_add_f32_e32 v76, v32, v33
	v_add_f32_e32 v73, v73, v10
	v_add_f32_e32 v74, v74, v18
	v_add_f32_e32 v75, v75, v26
	v_add_f32_e32 v76, v76, v34
	v_add_f32_e32 v73, v73, v11
	v_add_f32_e32 v74, v74, v19
	v_add_f32_e32 v75, v75, v27
	v_add_f32_e32 v76, v76, v35
	v_add_f32_e32 v73, v73, v12
	v_add_f32_e32 v74, v74, v20
	v_add_f32_e32 v75, v75, v28
	v_add_f32_e32 v76, v76, v36
	v_add_f32_e32 v73, v73, v13
	v_add_f32_e32 v74, v74, v21
	v_add_f32_e32 v75, v75, v29
	v_add_f32_e32 v76, v76, v37
	v_add_f32_dpp v73, v73, v73 quad_perm:[1,0,3,2] row_mask:0xf bank_mask:0xf bound_ctrl:1
	v_add_f32_dpp v74, v74, v74 quad_perm:[1,0,3,2] row_mask:0xf bank_mask:0xf bound_ctrl:1
	v_add_f32_dpp v75, v75, v75 quad_perm:[1,0,3,2] row_mask:0xf bank_mask:0xf bound_ctrl:1
	v_add_f32_dpp v76, v76, v76 quad_perm:[1,0,3,2] row_mask:0xf bank_mask:0xf bound_ctrl:1
	v_add_f32_dpp v73, v73, v73 quad_perm:[2,3,0,1] row_mask:0xf bank_mask:0xf bound_ctrl:1
	v_add_f32_dpp v74, v74, v74 quad_perm:[2,3,0,1] row_mask:0xf bank_mask:0xf bound_ctrl:1
	v_add_f32_dpp v75, v75, v75 quad_perm:[2,3,0,1] row_mask:0xf bank_mask:0xf bound_ctrl:1
	v_add_f32_dpp v76, v76, v76 quad_perm:[2,3,0,1] row_mask:0xf bank_mask:0xf bound_ctrl:1
	v_add_f32_dpp v73, v73, v73 row_half_mirror row_mask:0xf bank_mask:0xf bound_ctrl:1
	v_add_f32_dpp v74, v74, v74 row_half_mirror row_mask:0xf bank_mask:0xf bound_ctrl:1
	v_add_f32_dpp v75, v75, v75 row_half_mirror row_mask:0xf bank_mask:0xf bound_ctrl:1
	v_add_f32_dpp v76, v76, v76 row_half_mirror row_mask:0xf bank_mask:0xf bound_ctrl:1
	v_add_f32_dpp v73, v73, v73 row_mirror row_mask:0xf bank_mask:0xf bound_ctrl:1
	v_add_f32_dpp v74, v74, v74 row_mirror row_mask:0xf bank_mask:0xf bound_ctrl:1
	v_add_f32_dpp v75, v75, v75 row_mirror row_mask:0xf bank_mask:0xf bound_ctrl:1
	v_add_f32_dpp v76, v76, v76 row_mirror row_mask:0xf bank_mask:0xf bound_ctrl:1
	v_readlane_b32 s44, v73, 0
	v_readlane_b32 s45, v73, 16
	v_readlane_b32 s46, v73, 32
	v_readlane_b32 s47, v73, 48
	v_readlane_b32 s48, v74, 0
	v_readlane_b32 s49, v74, 16
	v_readlane_b32 s50, v74, 32
	v_readlane_b32 s51, v74, 48
	v_readlane_b32 s52, v75, 0
	v_readlane_b32 s53, v75, 16
	v_readlane_b32 s54, v75, 32
	v_readlane_b32 s55, v75, 48
	v_readlane_b32 s56, v76, 0
	v_readlane_b32 s57, v76, 16
	v_readlane_b32 s58, v76, 32
	v_readlane_b32 s59, v76, 48
	v_mov_b32_e32 v14, s44
	v_add_f32_e32 v14, s45, v14
	v_mov_b32_e32 v22, s48
	v_add_f32_e32 v22, s49, v22
	v_mov_b32_e32 v30, s52
	v_add_f32_e32 v30, s53, v30
	v_mov_b32_e32 v38, s56
	v_add_f32_e32 v38, s57, v38
	v_mov_b32_e32 v77, s46
	v_add_f32_e32 v77, s47, v77
	v_add_f32_e32 v14, v14, v77
	v_mov_b32_e32 v77, s50
	v_add_f32_e32 v77, s51, v77
	v_add_f32_e32 v22, v22, v77
	v_mov_b32_e32 v77, s54
	v_add_f32_e32 v77, s55, v77
	v_add_f32_e32 v30, v30, v77
	v_mov_b32_e32 v77, s58
	v_add_f32_e32 v77, s59, v77
	v_add_f32_e32 v38, v38, v77
	v_mul_f32_e32 v14, 0x3b2aaaab, v14
	v_mul_f32_e32 v22, 0x3b2aaaab, v22
	v_mul_f32_e32 v30, 0x3b2aaaab, v30
	v_mul_f32_e32 v38, 0x3b2aaaab, v38
	v_sub_f32_e32 v8, v8, v14
	v_sub_f32_e32 v16, v16, v22
	v_sub_f32_e32 v24, v24, v30
	v_sub_f32_e32 v32, v32, v38
	v_sub_f32_e32 v9, v9, v14
	v_sub_f32_e32 v17, v17, v22
	v_sub_f32_e32 v25, v25, v30
	v_sub_f32_e32 v33, v33, v38
	v_sub_f32_e32 v10, v10, v14
	v_sub_f32_e32 v18, v18, v22
	v_sub_f32_e32 v26, v26, v30
	v_sub_f32_e32 v34, v34, v38
	v_sub_f32_e32 v11, v11, v14
	v_sub_f32_e32 v19, v19, v22
	v_sub_f32_e32 v27, v27, v30
	v_sub_f32_e32 v35, v35, v38
	v_sub_f32_e32 v12, v12, v14
	v_sub_f32_e32 v20, v20, v22
	v_sub_f32_e32 v28, v28, v30
	v_sub_f32_e32 v36, v36, v38
	v_sub_f32_e32 v13, v13, v14
	v_sub_f32_e32 v21, v21, v22
	v_sub_f32_e32 v29, v29, v30
	v_sub_f32_e32 v37, v37, v38
	v_mul_f32_e32 v73, v8, v8
	v_mul_f32_e32 v74, v16, v16
	v_mul_f32_e32 v75, v24, v24
	v_mul_f32_e32 v76, v32, v32
	v_fmac_f32_e32 v73, v9, v9
	v_fmac_f32_e32 v74, v17, v17
	v_fmac_f32_e32 v75, v25, v25
	v_fmac_f32_e32 v76, v33, v33
	v_fmac_f32_e32 v73, v10, v10
	v_fmac_f32_e32 v74, v18, v18
	v_fmac_f32_e32 v75, v26, v26
	v_fmac_f32_e32 v76, v34, v34
	v_fmac_f32_e32 v73, v11, v11
	v_fmac_f32_e32 v74, v19, v19
	v_fmac_f32_e32 v75, v27, v27
	v_fmac_f32_e32 v76, v35, v35
	v_fmac_f32_e32 v73, v12, v12
	v_fmac_f32_e32 v74, v20, v20
	v_fmac_f32_e32 v75, v28, v28
	v_fmac_f32_e32 v76, v36, v36
	v_fmac_f32_e32 v73, v13, v13
	v_fmac_f32_e32 v74, v21, v21
	v_fmac_f32_e32 v75, v29, v29
	v_fmac_f32_e32 v76, v37, v37
	v_add_f32_dpp v73, v73, v73 quad_perm:[1,0,3,2] row_mask:0xf bank_mask:0xf bound_ctrl:1
	v_add_f32_dpp v74, v74, v74 quad_perm:[1,0,3,2] row_mask:0xf bank_mask:0xf bound_ctrl:1
	v_add_f32_dpp v75, v75, v75 quad_perm:[1,0,3,2] row_mask:0xf bank_mask:0xf bound_ctrl:1
	v_add_f32_dpp v76, v76, v76 quad_perm:[1,0,3,2] row_mask:0xf bank_mask:0xf bound_ctrl:1
	v_add_f32_dpp v73, v73, v73 quad_perm:[2,3,0,1] row_mask:0xf bank_mask:0xf bound_ctrl:1
	v_add_f32_dpp v74, v74, v74 quad_perm:[2,3,0,1] row_mask:0xf bank_mask:0xf bound_ctrl:1
	v_add_f32_dpp v75, v75, v75 quad_perm:[2,3,0,1] row_mask:0xf bank_mask:0xf bound_ctrl:1
	v_add_f32_dpp v76, v76, v76 quad_perm:[2,3,0,1] row_mask:0xf bank_mask:0xf bound_ctrl:1
	v_add_f32_dpp v73, v73, v73 row_half_mirror row_mask:0xf bank_mask:0xf bound_ctrl:1
	v_add_f32_dpp v74, v74, v74 row_half_mirror row_mask:0xf bank_mask:0xf bound_ctrl:1
	v_add_f32_dpp v75, v75, v75 row_half_mirror row_mask:0xf bank_mask:0xf bound_ctrl:1
	v_add_f32_dpp v76, v76, v76 row_half_mirror row_mask:0xf bank_mask:0xf bound_ctrl:1
	v_add_f32_dpp v73, v73, v73 row_mirror row_mask:0xf bank_mask:0xf bound_ctrl:1
	v_add_f32_dpp v74, v74, v74 row_mirror row_mask:0xf bank_mask:0xf bound_ctrl:1
	v_add_f32_dpp v75, v75, v75 row_mirror row_mask:0xf bank_mask:0xf bound_ctrl:1
	v_add_f32_dpp v76, v76, v76 row_mirror row_mask:0xf bank_mask:0xf bound_ctrl:1
	v_readlane_b32 s44, v73, 0
	v_readlane_b32 s45, v73, 16
	v_readlane_b32 s46, v73, 32
	v_readlane_b32 s47, v73, 48
	v_readlane_b32 s48, v74, 0
	v_readlane_b32 s49, v74, 16
	v_readlane_b32 s50, v74, 32
	v_readlane_b32 s51, v74, 48
	v_readlane_b32 s52, v75, 0
	v_readlane_b32 s53, v75, 16
	v_readlane_b32 s54, v75, 32
	v_readlane_b32 s55, v75, 48
	v_readlane_b32 s56, v76, 0
	v_readlane_b32 s57, v76, 16
	v_readlane_b32 s58, v76, 32
	v_readlane_b32 s59, v76, 48
	v_mov_b32_e32 v15, s44
	v_add_f32_e32 v15, s45, v15
	v_mov_b32_e32 v23, s48
	v_add_f32_e32 v23, s49, v23
	v_mov_b32_e32 v31, s52
	v_add_f32_e32 v31, s53, v31
	v_mov_b32_e32 v39, s56
	v_add_f32_e32 v39, s57, v39
	v_mov_b32_e32 v77, s46
	v_add_f32_e32 v77, s47, v77
	v_add_f32_e32 v15, v15, v77
	v_mov_b32_e32 v77, s50
	v_add_f32_e32 v77, s51, v77
	v_add_f32_e32 v23, v23, v77
	v_mov_b32_e32 v77, s54
	v_add_f32_e32 v77, s55, v77
	v_add_f32_e32 v31, v31, v77
	v_mov_b32_e32 v77, s58
	v_add_f32_e32 v77, s59, v77
	v_add_f32_e32 v39, v39, v77
	v_mov_b32_e32 v14, 0x3727c5ac
	v_mov_b32_e32 v22, 0x3727c5ac
	v_mov_b32_e32 v30, 0x3727c5ac
	v_mov_b32_e32 v38, 0x3727c5ac
	v_fmac_f32_e32 v14, 0x3b2aaaab, v15
	v_fmac_f32_e32 v22, 0x3b2aaaab, v23
	v_fmac_f32_e32 v30, 0x3b2aaaab, v31
	v_fmac_f32_e32 v38, 0x3b2aaaab, v39
	v_rsq_f32_e32 v15, v14
	v_rsq_f32_e32 v23, v22
	v_rsq_f32_e32 v31, v30
	v_rsq_f32_e32 v39, v38
	v_mul_f32_e32 v8, v8, v15
	v_mul_f32_e32 v16, v16, v23
	v_mul_f32_e32 v24, v24, v31
	v_mul_f32_e32 v32, v32, v39
	v_mul_f32_e32 v9, v9, v15
	v_mul_f32_e32 v17, v17, v23
	v_mul_f32_e32 v25, v25, v31
	v_mul_f32_e32 v33, v33, v39
	v_mul_f32_e32 v10, v10, v15
	v_mul_f32_e32 v18, v18, v23
	v_mul_f32_e32 v26, v26, v31
	v_mul_f32_e32 v34, v34, v39
	v_mul_f32_e32 v11, v11, v15
	v_mul_f32_e32 v19, v19, v23
	v_mul_f32_e32 v27, v27, v31
	v_mul_f32_e32 v35, v35, v39
	v_mul_f32_e32 v12, v12, v15
	v_mul_f32_e32 v20, v20, v23
	v_mul_f32_e32 v28, v28, v31
	v_mul_f32_e32 v36, v36, v39
	v_mul_f32_e32 v13, v13, v15
	v_mul_f32_e32 v21, v21, v23
	v_mul_f32_e32 v29, v29, v31
	v_mul_f32_e32 v37, v37, v39
	v_fma_f32 v8, v56, v8, v62
	v_fma_f32 v16, v56, v16, v62
	v_fma_f32 v24, v56, v24, v62
	v_fma_f32 v32, v56, v32, v62
	v_fma_f32 v9, v57, v9, v63
	v_fma_f32 v17, v57, v17, v63
	v_fma_f32 v25, v57, v25, v63
	v_fma_f32 v33, v57, v33, v63
	v_fma_f32 v10, v58, v10, v64
	v_fma_f32 v18, v58, v18, v64
	v_fma_f32 v26, v58, v26, v64
	v_fma_f32 v34, v58, v34, v64
	v_fma_f32 v11, v59, v11, v65
	v_fma_f32 v19, v59, v19, v65
	v_fma_f32 v27, v59, v27, v65
	v_fma_f32 v35, v59, v35, v65
	v_fma_f32 v12, v60, v12, v66
	v_fma_f32 v20, v60, v20, v66
	v_fma_f32 v28, v60, v28, v66
	v_fma_f32 v36, v60, v36, v66
	v_fma_f32 v13, v61, v13, v67
	v_fma_f32 v21, v61, v21, v67
	v_fma_f32 v29, v61, v29, v67
	v_fma_f32 v37, v61, v37, v67
	v_cvt_pk_bf16_f32 v40, v8, v9
	v_cvt_pk_bf16_f32 v44, v16, v17
	v_cvt_pk_bf16_f32 v48, v24, v25
	v_cvt_pk_bf16_f32 v52, v32, v33
	v_cvt_pk_bf16_f32 v41, v10, v11
	v_cvt_pk_bf16_f32 v45, v18, v19
	v_cvt_pk_bf16_f32 v49, v26, v27
	v_cvt_pk_bf16_f32 v53, v34, v35
	v_cvt_pk_bf16_f32 v42, v12, v13
	v_cvt_pk_bf16_f32 v46, v20, v21
	v_cvt_pk_bf16_f32 v50, v28, v29
	v_cvt_pk_bf16_f32 v54, v36, v37
	global_store_dwordx3 v70, v[40:42], s[42:43]
	global_store_dwordx3 v70, v[44:46], s[42:43] offset:768
	global_store_dwordx3 v70, v[48:50], s[42:43] offset:1536
	global_store_dwordx3 v70, v[52:54], s[42:43] offset:2304
	s_branch .LBB1_60

	.amdhsa_kernel _Z12front_kernel9FrontArgs8PrepArgs8FragArgs
		.amdhsa_group_segment_fixed_size 50688
		.amdhsa_private_segment_fixed_size 0
		.amdhsa_kernarg_size 760
		.amdhsa_user_sgpr_count 2
		.amdhsa_user_sgpr_dispatch_ptr 0
		.amdhsa_user_sgpr_queue_ptr 0
		.amdhsa_user_sgpr_kernarg_segment_ptr 1
		.amdhsa_user_sgpr_dispatch_id 0
		.amdhsa_user_sgpr_kernarg_preload_length 0
		.amdhsa_user_sgpr_kernarg_preload_offset 0
		.amdhsa_user_sgpr_private_segment_size 0
		.amdhsa_uses_dynamic_stack 0
		.amdhsa_enable_private_segment 0
		.amdhsa_system_sgpr_workgroup_id_x 1
		.amdhsa_system_sgpr_workgroup_id_y 0
		.amdhsa_system_sgpr_workgroup_id_z 0
		.amdhsa_system_sgpr_workgroup_info 0
		.amdhsa_system_vgpr_workitem_id 0
		.amdhsa_next_free_vgpr 80
		.amdhsa_next_free_sgpr 91
		.amdhsa_accum_offset 80
		.amdhsa_reserve_vcc 1
		.amdhsa_float_round_mode_32 0
		.amdhsa_float_round_mode_16_64 0
		.amdhsa_float_denorm_mode_32 3
		.amdhsa_float_denorm_mode_16_64 3
		.amdhsa_dx10_clamp 1
		.amdhsa_ieee_mode 1
		.amdhsa_fp16_overflow 0
		.amdhsa_tg_split 0
		.amdhsa_exception_fp_ieee_invalid_op 0
		.amdhsa_exception_fp_denorm_src 0
		.amdhsa_exception_fp_ieee_div_zero 0
		.amdhsa_exception_fp_ieee_overflow 0
		.amdhsa_exception_fp_ieee_underflow 0
		.amdhsa_exception_fp_ieee_inexact 0
		.amdhsa_exception_int_div_zero 0
	.end_amdhsa_kernel

amdhsa.kernels:
  - .agpr_count:     0
    .args:
      - .offset:         0
        .size:           4
        .value_kind:     by_value
      - .actual_access:  read_only
        .address_space:  global
        .offset:         8
        .size:           8
        .value_kind:     global_buffer
      - .actual_access:  read_only
        .address_space:  global
        .offset:         16
        .size:           8
        .value_kind:     global_buffer
      - .actual_access:  read_only
        .address_space:  global
        .offset:         24
        .size:           8
        .value_kind:     global_buffer
      - .actual_access:  read_only
        .address_space:  global
        .offset:         32
        .size:           8
        .value_kind:     global_buffer
      - .offset:         40
        .size:           4
        .value_kind:     by_value
      - .actual_access:  read_only
        .address_space:  global
        .offset:         48
        .size:           8
        .value_kind:     global_buffer
      - .actual_access:  read_only
        .address_space:  global
        .offset:         56
        .size:           8
        .value_kind:     global_buffer
      - .offset:         64
        .size:           4
        .value_kind:     by_value
      - .actual_access:  write_only
        .address_space:  global
        .offset:         72
        .size:           8
        .value_kind:     global_buffer
      - .offset:         80
        .size:           4
        .value_kind:     by_value
    .group_segment_fixed_size: 128
    .kernarg_segment_align: 8
    .kernarg_segment_size: 84
    .language:       OpenCL C
    .language_version:
      - 2
      - 0
    .max_flat_workgroup_size: 256
    .name:           _Z12graph_kerneliPKfS0_S0_PKtiS2_S2_iPti
    .private_segment_fixed_size: 0
    .sgpr_count:     48
    .sgpr_spill_count: 0
    .symbol:         _Z12graph_kerneliPKfS0_S0_PKtiS2_S2_iPti.kd
    .uniform_work_group_size: 1
    .uses_dynamic_stack: false
    .vgpr_count:     75
    .vgpr_spill_count: 0
    .wavefront_size: 64
  - .agpr_count:     0
    .args:
      - .offset:         0
        .size:           96
        .value_kind:     by_value
      - .offset:         96
        .size:           336
        .value_kind:     by_value
      - .offset:         432
        .size:           328
        .value_kind:     by_value
    .group_segment_fixed_size: 50688
    .kernarg_segment_align: 8
    .kernarg_segment_size: 760
    .language:       OpenCL C
    .language_version:
      - 2
      - 0
    .max_flat_workgroup_size: 512
    .name:           _Z12front_kernel9FrontArgs8PrepArgs8FragArgs
    .private_segment_fixed_size: 0
    .sgpr_count:     58
    .sgpr_spill_count: 0
    .symbol:         _Z12front_kernel9FrontArgs8PrepArgs8FragArgs.kd
    .uniform_work_group_size: 1
    .uses_dynamic_stack: false
    .vgpr_count:     80
    .vgpr_spill_count: 0
    .wavefront_size: 64
  - .agpr_count:     0
    .args:
      - .offset:         0
        .size:           144
        .value_kind:     by_value
    .group_segment_fixed_size: 131072
    .kernarg_segment_align: 8
    .kernarg_segment_size: 144
    .language:       OpenCL C
    .language_version:
      - 2
      - 0
    .max_flat_workgroup_size: 512
    .name:           _Z13gemm8p_kernel5GArgs
    .private_segment_fixed_size: 0
    .sgpr_count:     42
    .sgpr_spill_count: 0
    .symbol:         _Z13gemm8p_kernel5GArgs.kd
    .uniform_work_group_size: 1
    .uses_dynamic_stack: false
    .vgpr_count:     250
    .vgpr_spill_count: 0
    .wavefront_size: 64
  - .agpr_count:     0
    .args:
      - .actual_access:  read_only
        .address_space:  global
        .offset:         0
        .size:           8
        .value_kind:     global_buffer
      - .offset:         8
        .size:           4
        .value_kind:     by_value
      - .address_space:  global
        .offset:         16
        .size:           8
        .value_kind:     global_buffer
      - .offset:         24
        .size:           4
        .value_kind:     by_value
      - .address_space:  global
        .offset:         32
        .size:           8
        .value_kind:     global_buffer
      - .offset:         40
        .size:           4
        .value_kind:     by_value
      - .actual_access:  write_only
        .address_space:  global
        .offset:         48
        .size:           8
        .value_kind:     global_buffer
      - .offset:         56
        .size:           4
        .value_kind:     by_value
      - .offset:         64
        .size:           112
        .value_kind:     by_value
    .group_segment_fixed_size: 83968
    .kernarg_segment_align: 8
    .kernarg_segment_size: 176
    .language:       OpenCL C
    .language_version:
      - 2
      - 0
    .max_flat_workgroup_size: 512
    .name:           _Z11attn_kernelPKtiS0_iS0_iPti6CoArgs
    .private_segment_fixed_size: 0
    .sgpr_count:     74
    .sgpr_spill_count: 0
    .symbol:         _Z11attn_kernelPKtiS0_iS0_iPti6CoArgs.kd
    .uniform_work_group_size: 1
    .uses_dynamic_stack: false
    .vgpr_count:     218
    .vgpr_spill_count: 0
    .wavefront_size: 64
  - .agpr_count:     0
    .args:
      - .offset:         0
        .size:           144
        .value_kind:     by_value
    .group_segment_fixed_size: 77312
    .kernarg_segment_align: 8
    .kernarg_segment_size: 144
    .language:       OpenCL C
    .language_version:
      - 2
      - 0
    .max_flat_workgroup_size: 512
    .name:           _Z12chain_kernelILi0EEv9ChainArgs
    .private_segment_fixed_size: 0
    .sgpr_count:     35
    .sgpr_spill_count: 0
    .symbol:         _Z12chain_kernelILi0EEv9ChainArgs.kd
    .uniform_work_group_size: 1
    .uses_dynamic_stack: false
    .vgpr_count:     224
    .vgpr_spill_count: 0
    .wavefront_size: 64
  - .agpr_count:     0
    .args:
      - .offset:         0
        .size:           144
        .value_kind:     by_value
    .group_segment_fixed_size: 77312
    .kernarg_segment_align: 8
    .kernarg_segment_size: 144
    .language:       OpenCL C
    .language_version:
      - 2
      - 0
    .max_flat_workgroup_size: 512
    .name:           _Z12chain_kernelILi1EEv9ChainArgs
    .private_segment_fixed_size: 0
    .sgpr_count:     35
    .sgpr_spill_count: 0
    .symbol:         _Z12chain_kernelILi1EEv9ChainArgs.kd
    .uniform_work_group_size: 1
    .uses_dynamic_stack: false
    .vgpr_count:     210
    .vgpr_spill_count: 0
    .wavefront_size: 64
